# baseline (speedup 1.0000x reference)
_Z6k_gramILi0EEvPK15HIP_vector_typeIjLj4EEPyPf:
	s_load_dwordx4 s[8:11], s[0:1], 0x0
	s_load_dwordx2 s[4:5], s[0:1], 0x10
	s_lshl_b32 s0, s2, 2
	s_and_b32 s0, s0, 28
	s_ashr_i32 s1, s2, 6
	s_add_i32 s16, s0, s1
	v_readfirstlane_b32 s23, v0
	s_ashr_i32 s17, s16, 31
	s_lshr_b32 s21, s23, 6
	s_bfe_u32 s18, s23, 0x20006
	s_lshr_b32 s22, s2, 3
	s_bfe_u32 s20, s2, 0x30003
	s_lshl_b64 s[0:1], s[16:17], 20
	s_waitcnt lgkmcnt(0)
	s_add_u32 s12, s8, s0
	v_mov_b32_e32 v1, 0x20000
	s_addc_u32 s0, s9, s1
	s_lshl_b32 s1, s20, 2
	v_lshl_or_b32 v1, v0, 2, v1
	v_bfrev_b32_e32 v2, 1
	s_cmp_lt_u32 s20, 4
	ds_write_b32 v1, v2
	s_mov_b32 s24, 4
	s_mov_b32 s15, 0x20000
	s_and_b32 s13, s0, 0xffff
	s_mov_b32 s14, 0x100000
	v_lshlrev_b32_e32 v166, 4, v0
	s_lshl_b32 s25, s21, 10
	s_lshl_b32 s0, s20, 17
	s_mov_b32 m0, s25
	s_nop 0
	buffer_load_dwordx4 v166, s[12:15], s0 offen lds
	s_add_i32 s27, s25, 0x4000
	s_or_b32 s2, s0, 0x8000
	s_mov_b32 m0, s27
	s_nop 0
	buffer_load_dwordx4 v166, s[12:15], s2 offen lds
	s_add_i32 s34, s25, 0x10000
	s_or_b32 s2, s0, 0x10000
	s_mov_b32 m0, s34
	s_nop 0
	buffer_load_dwordx4 v166, s[12:15], s2 offen lds
	s_add_i32 s36, s25, 0x14000
	s_or_b32 s2, s0, 0x18000
	s_mov_b32 m0, s36
	s_nop 0
	buffer_load_dwordx4 v166, s[12:15], s2 offen lds
	s_add_i32 s26, s25, 0x2000
	s_or_b32 s2, s0, 0x2000
	s_mov_b32 m0, s26
	s_nop 0
	buffer_load_dwordx4 v166, s[12:15], s2 offen lds
	s_add_i32 s28, s25, 0x6000
	s_or_b32 s2, s0, 0xa000
	s_mov_b32 m0, s28
	s_nop 0
	buffer_load_dwordx4 v166, s[12:15], s2 offen lds
	s_add_i32 s35, s25, 0x12000
	s_or_b32 s2, s0, 0x12000
	s_mov_b32 m0, s35
	s_nop 0
	buffer_load_dwordx4 v166, s[12:15], s2 offen lds
	s_add_i32 s37, s25, 0x16000
	s_or_b32 s2, s0, 0x1a000
	s_mov_b32 m0, s37
	s_nop 0
	buffer_load_dwordx4 v166, s[12:15], s2 offen lds
	s_add_i32 s29, s25, 0x8000
	s_or_b32 s2, s0, 0x4000
	s_mov_b32 m0, s29
	s_nop 0
	buffer_load_dwordx4 v166, s[12:15], s2 offen lds
	s_add_i32 s31, s25, 0xc000
	s_or_b32 s2, s0, 0xc000
	s_mov_b32 m0, s31
	s_nop 0
	buffer_load_dwordx4 v166, s[12:15], s2 offen lds
	s_add_i32 s38, s25, 0x18000
	s_or_b32 s2, s0, 0x14000
	s_mov_b32 m0, s38
	s_nop 0
	buffer_load_dwordx4 v166, s[12:15], s2 offen lds
	s_add_i32 s40, s25, 0x1c000
	s_or_b32 s2, s0, 0x1c000
	s_mov_b32 m0, s40
	s_nop 0
	buffer_load_dwordx4 v166, s[12:15], s2 offen lds
	s_add_i32 s30, s25, 0xa000
	s_or_b32 s2, s0, 0x6000
	s_mov_b32 m0, s30
	s_nop 0
	buffer_load_dwordx4 v166, s[12:15], s2 offen lds
	s_add_i32 s33, s25, 0xe000
	s_or_b32 s2, s0, 0xe000
	s_mov_b32 m0, s33
	s_nop 0
	buffer_load_dwordx4 v166, s[12:15], s2 offen lds
	s_add_i32 s39, s25, 0x1a000
	s_or_b32 s2, s0, 0x16000
	s_mov_b32 m0, s39
	s_nop 0
	buffer_load_dwordx4 v166, s[12:15], s2 offen lds
	s_add_i32 s42, s25, 0x1e000
	s_or_b32 s2, s0, 0x1e000
	s_mov_b32 m0, s42
	s_nop 0
	buffer_load_dwordx4 v166, s[12:15], s2 offen lds
	s_lshl_b32 s0, s23, 9
	s_lshl_b32 s2, s23, 8
	v_and_b32_e32 v167, 15, v0
	v_bfe_u32 v160, v0, 4, 2
	s_and_b32 s0, s0, 0x10000
	s_and_b32 s2, s2, 0x4000
	v_lshlrev_b32_e32 v128, 9, v160
	v_lshlrev_b32_e32 v129, 4, v167
	s_or_b32 s0, s0, s2
	v_or3_b32 v124, s0, v128, v129
	s_waitcnt vmcnt(12)
	s_waitcnt lgkmcnt(0)
	s_barrier
	s_lshr_b32 s41, s23, 8
	s_lshl_b32 s0, s41, 14
	s_lshl_b32 s50, s24, 2
	v_or3_b32 v168, s0, v128, v129
	s_or_b32 s43, s18, s1
	s_lshl_b32 s0, s16, 10
	s_lshl_b32 s1, s43, 5
	ds_read_b128 v[128:131], v168
	ds_read_b128 v[132:135], v168 offset:256
	ds_read_b128 v[136:139], v168 offset:2048
	ds_read_b128 v[140:143], v168 offset:2304
	s_or_b32 s0, s1, s0
	v_or_b32_e32 v144, s0, v167
	v_lshlrev_b32_e32 v146, 2, v160
	v_ashrrev_i32_e32 v145, 31, v144
	v_lshl_add_u64 v[164:165], v[144:145], 2, s[4:5]
	v_or_b32_e32 v144, 1, v146
	v_cmp_eq_u32_e64 s[2:3], v144, v167
	v_or_b32_e32 v144, 2, v146
	v_cmp_eq_u32_e64 s[4:5], v144, v167
	v_or_b32_e32 v144, 3, v146
	s_add_i32 s44, s50, 3
	s_lshl_b32 s45, s22, 2
	v_cmp_eq_u32_e64 s[0:1], v146, v167
	v_cmp_eq_u32_e64 s[6:7], v144, v167
	v_add_u32_e32 v169, 0x10000, v168
	v_add_u32_e32 v170, 0x10100, v168
	v_add_u32_e32 v171, 0x10800, v168
	v_add_u32_e32 v172, 0x10900, v168
	s_and_b32 s8, s45, 28
	s_add_i32 s8, s8, s41
	s_lshl_b32 s19, s8, 1
	s_or_b32 s51, s19, 1
	v_mov_b32_e32 v234, s19
	v_mov_b32_e32 v235, s51
	s_and_b32 s46, s21, 3
	s_lshl_b32 s46, s46, 5
	v_lshl_or_b32 v173, v160, 3, s46
	s_lshl_b32 s47, s41, 7
	s_mov_b32 s48, 0
	s_movk_i32 s49, 0xffc0
	v_add_u32_e32 v174, 0x11000, v168
	v_add_u32_e32 v175, 0x11100, v168
	v_add_u32_e32 v176, 0x11800, v168
	v_add_u32_e32 v177, 0x11900, v168
	v_add_u32_e32 v178, 0x12000, v168
	v_add_u32_e32 v179, 0x12100, v168
	v_add_u32_e32 v180, 0x12800, v168
	v_add_u32_e32 v181, 0x12900, v168
	v_add_u32_e32 v182, 0x13000, v168
	v_add_u32_e32 v183, 0x13100, v168
	v_add_u32_e32 v184, 0x13800, v168
	v_add_u32_e32 v185, 0x13900, v168
	v_add_u32_e32 v186, 0x18000, v168
	v_add_u32_e32 v187, 0x18100, v168
	v_add_u32_e32 v188, 0x18800, v168
	v_add_u32_e32 v189, 0x18900, v168
	v_add_u32_e32 v190, 0x19000, v168
	v_add_u32_e32 v191, 0x19100, v168
	v_add_u32_e32 v192, 0x19800, v168
	v_add_u32_e32 v193, 0x19900, v168
	v_add_u32_e32 v194, 0x1a000, v168
	v_add_u32_e32 v195, 0x1a100, v168
	v_add_u32_e32 v196, 0x1a800, v168
	v_add_u32_e32 v197, 0x1a900, v168
	v_add_u32_e32 v198, 0x1b000, v168
	v_add_u32_e32 v199, 0x1b100, v168
	v_add_u32_e32 v200, 0x1b800, v168
	v_add_u32_e32 v201, 0x1b900, v168
	ds_read_b128 v[0:3], v124
	ds_read_b128 v[4:7], v124 offset:256
	ds_read_b128 v[8:11], v124 offset:2048
	ds_read_b128 v[12:15], v124 offset:2304
	ds_read_b128 v[144:147], v168
	ds_read_b128 v[148:151], v168 offset:256
	ds_read_b128 v[152:155], v168 offset:2048
	ds_read_b128 v[156:159], v168 offset:2304
	ds_read_b128 v[224:227], v168 offset:4096
	s_waitcnt lgkmcnt(4)
	v_mfma_f32_16x16x32_bf16 v[208:211], v[0:3], v[144:147], 0
	v_mfma_f32_16x16x32_bf16 v[212:215], v[4:7], v[144:147], 0
	ds_read_b128 v[228:231], v168 offset:4352
	ds_read_b128 v[16:19], v124 offset:4096
	ds_read_b128 v[20:23], v124 offset:4352
	s_waitcnt lgkmcnt(6)
	v_mfma_f32_16x16x32_bf16 v[216:219], v[0:3], v[148:151], 0
	v_mfma_f32_16x16x32_bf16 v[220:223], v[4:7], v[148:151], 0
	ds_read_b128 v[144:147], v168 offset:6144
	s_waitcnt lgkmcnt(6)
	v_mfma_f32_16x16x32_bf16 v[208:211], v[8:11], v[152:155], v[208:211]
	v_mfma_f32_16x16x32_bf16 v[212:215], v[12:15], v[152:155], v[212:215]
	ds_read_b128 v[148:151], v168 offset:6400
	ds_read_b128 v[24:27], v124 offset:6144
	ds_read_b128 v[28:31], v124 offset:6400
	s_waitcnt lgkmcnt(8)
	v_mfma_f32_16x16x32_bf16 v[216:219], v[8:11], v[156:159], v[216:219]
	v_mfma_f32_16x16x32_bf16 v[220:223], v[12:15], v[156:159], v[220:223]
	s_waitcnt lgkmcnt(4)
	v_mfma_f32_16x16x32_bf16 v[208:211], v[16:19], v[224:227], v[208:211]
	v_mfma_f32_16x16x32_bf16 v[212:215], v[20:23], v[224:227], v[212:215]
	v_mfma_f32_16x16x32_bf16 v[216:219], v[16:19], v[228:231], v[216:219]
	v_mfma_f32_16x16x32_bf16 v[220:223], v[20:23], v[228:231], v[220:223]
	s_waitcnt lgkmcnt(0)
	v_mfma_f32_16x16x32_bf16 v[208:211], v[24:27], v[144:147], v[208:211]
	v_mfma_f32_16x16x32_bf16 v[212:215], v[28:31], v[144:147], v[212:215]
	v_mfma_f32_16x16x32_bf16 v[216:219], v[24:27], v[148:151], v[216:219]
	v_mfma_f32_16x16x32_bf16 v[220:223], v[28:31], v[148:151], v[220:223]
	s_waitcnt vmcnt(8)
	s_barrier
	ds_read_b128 v[152:155], v168 offset:8192
	ds_read_b128 v[156:159], v168 offset:8448
	ds_read_b128 v[224:227], v168 offset:10240
	ds_read_b128 v[228:231], v168 offset:10496
	ds_read_b128 v[144:147], v168 offset:12288
	ds_read_b128 v[32:35], v124 offset:8192
	ds_read_b128 v[36:39], v124 offset:8448
	ds_read_b128 v[40:43], v124 offset:10240
	ds_read_b128 v[44:47], v124 offset:10496
	s_waitcnt lgkmcnt(2)
	v_mfma_f32_16x16x32_bf16 v[208:211], v[32:35], v[152:155], v[208:211]
	v_mfma_f32_16x16x32_bf16 v[212:215], v[36:39], v[152:155], v[212:215]
	ds_read_b128 v[148:151], v168 offset:12544
	ds_read_b128 v[48:51], v124 offset:12288
	ds_read_b128 v[52:55], v124 offset:12544
	v_mfma_f32_16x16x32_bf16 v[216:219], v[32:35], v[156:159], v[216:219]
	v_mfma_f32_16x16x32_bf16 v[220:223], v[36:39], v[156:159], v[220:223]
	ds_read_b128 v[152:155], v168 offset:14336
	s_waitcnt lgkmcnt(4)
	v_mfma_f32_16x16x32_bf16 v[208:211], v[40:43], v[224:227], v[208:211]
	v_mfma_f32_16x16x32_bf16 v[212:215], v[44:47], v[224:227], v[212:215]
	ds_read_b128 v[156:159], v168 offset:14592
	ds_read_b128 v[56:59], v124 offset:14336
	ds_read_b128 v[60:63], v124 offset:14592
	v_mfma_f32_16x16x32_bf16 v[216:219], v[40:43], v[228:231], v[216:219]
	v_mfma_f32_16x16x32_bf16 v[220:223], v[44:47], v[228:231], v[220:223]
	s_waitcnt lgkmcnt(4)
	v_mfma_f32_16x16x32_bf16 v[208:211], v[48:51], v[144:147], v[208:211]
	v_mfma_f32_16x16x32_bf16 v[212:215], v[52:55], v[144:147], v[212:215]
	v_mfma_f32_16x16x32_bf16 v[216:219], v[48:51], v[148:151], v[216:219]
	v_mfma_f32_16x16x32_bf16 v[220:223], v[52:55], v[148:151], v[220:223]
	s_waitcnt lgkmcnt(0)
	v_mfma_f32_16x16x32_bf16 v[208:211], v[56:59], v[152:155], v[208:211]
	v_mfma_f32_16x16x32_bf16 v[212:215], v[60:63], v[152:155], v[212:215]
	v_mfma_f32_16x16x32_bf16 v[216:219], v[56:59], v[156:159], v[216:219]
	v_mfma_f32_16x16x32_bf16 v[220:223], v[60:63], v[156:159], v[220:223]
	s_barrier
	s_add_i32 s60, s45, 4
	s_and_b32 s60, s60, 28
	s_lshl_b32 s60, s60, 15
	ds_read_b128 v[144:147], v169
	ds_read_b128 v[148:151], v169 offset:256
	ds_read_b128 v[152:155], v169 offset:2048
	ds_read_b128 v[156:159], v169 offset:2304
	ds_read_b128 v[224:227], v169 offset:4096
	s_waitcnt lgkmcnt(4)
	v_mfma_f32_16x16x32_bf16 v[136:139], v[0:3], v[144:147], 0
	v_mfma_f32_16x16x32_bf16 v[128:131], v[4:7], v[144:147], 0
	ds_read_b128 v[228:231], v169 offset:4352
	s_waitcnt lgkmcnt(4)
	v_mfma_f32_16x16x32_bf16 v[140:143], v[0:3], v[148:151], 0
	v_mfma_f32_16x16x32_bf16 v[132:135], v[4:7], v[148:151], 0
	ds_read_b128 v[144:147], v169 offset:6144
	s_waitcnt lgkmcnt(4)
	v_mfma_f32_16x16x32_bf16 v[136:139], v[8:11], v[152:155], v[136:139]
	v_mfma_f32_16x16x32_bf16 v[128:131], v[12:15], v[152:155], v[128:131]
	ds_read_b128 v[148:151], v169 offset:6400
	s_waitcnt lgkmcnt(4)
	v_mfma_f32_16x16x32_bf16 v[140:143], v[8:11], v[156:159], v[140:143]
	v_mfma_f32_16x16x32_bf16 v[132:135], v[12:15], v[156:159], v[132:135]
	ds_read_b128 v[152:155], v169 offset:8192
	s_waitcnt lgkmcnt(4)
	v_mfma_f32_16x16x32_bf16 v[136:139], v[16:19], v[224:227], v[136:139]
	v_mfma_f32_16x16x32_bf16 v[128:131], v[20:23], v[224:227], v[128:131]
	ds_read_b128 v[156:159], v169 offset:8448
	s_waitcnt lgkmcnt(4)
	v_mfma_f32_16x16x32_bf16 v[140:143], v[16:19], v[228:231], v[140:143]
	v_mfma_f32_16x16x32_bf16 v[132:135], v[20:23], v[228:231], v[132:135]
	ds_read_b128 v[224:227], v169 offset:10240
	s_waitcnt lgkmcnt(4)
	v_mfma_f32_16x16x32_bf16 v[136:139], v[24:27], v[144:147], v[136:139]
	v_mfma_f32_16x16x32_bf16 v[128:131], v[28:31], v[144:147], v[128:131]
	ds_read_b128 v[228:231], v169 offset:10496
	s_waitcnt lgkmcnt(4)
	v_mfma_f32_16x16x32_bf16 v[140:143], v[24:27], v[148:151], v[140:143]
	v_mfma_f32_16x16x32_bf16 v[132:135], v[28:31], v[148:151], v[132:135]
	ds_read_b128 v[144:147], v169 offset:12288
	s_waitcnt vmcnt(4)
	s_barrier
	s_waitcnt lgkmcnt(4)
	v_mfma_f32_16x16x32_bf16 v[136:139], v[32:35], v[152:155], v[136:139]
	v_mfma_f32_16x16x32_bf16 v[128:131], v[36:39], v[152:155], v[128:131]
	ds_read_b128 v[148:151], v169 offset:12544
	ds_read_b128 v[64:67], v124 offset:32768
	ds_read_b128 v[68:71], v124 offset:33024
	s_waitcnt lgkmcnt(6)
	v_mfma_f32_16x16x32_bf16 v[140:143], v[32:35], v[156:159], v[140:143]
	s_mov_b32 s61, s60
	s_mov_b32 m0, s25
	s_nop 0
	buffer_load_dwordx4 v166, s[12:15], s61 offen lds
	v_mfma_f32_16x16x32_bf16 v[132:135], v[36:39], v[156:159], v[132:135]
	ds_read_b128 v[152:155], v169 offset:14336
	s_waitcnt lgkmcnt(6)
	v_mfma_f32_16x16x32_bf16 v[136:139], v[40:43], v[224:227], v[136:139]
	v_mfma_f32_16x16x32_bf16 v[128:131], v[44:47], v[224:227], v[128:131]
	ds_read_b128 v[156:159], v169 offset:14592
	ds_read_b128 v[72:75], v124 offset:34816
	ds_read_b128 v[76:79], v124 offset:35072
	s_waitcnt lgkmcnt(8)
	v_mfma_f32_16x16x32_bf16 v[140:143], v[40:43], v[228:231], v[140:143]
	s_or_b32 s61, s60, 0x2000
	s_mov_b32 m0, s26
	s_nop 0
	buffer_load_dwordx4 v166, s[12:15], s61 offen lds
	v_mfma_f32_16x16x32_bf16 v[132:135], v[44:47], v[228:231], v[132:135]
	s_waitcnt lgkmcnt(7)
	v_mfma_f32_16x16x32_bf16 v[136:139], v[48:51], v[144:147], v[136:139]
	v_mfma_f32_16x16x32_bf16 v[128:131], v[52:55], v[144:147], v[128:131]
	ds_read_b128 v[80:83], v124 offset:36864
	ds_read_b128 v[84:87], v124 offset:37120
	s_waitcnt lgkmcnt(8)
	v_mfma_f32_16x16x32_bf16 v[140:143], v[48:51], v[148:151], v[140:143]
	s_or_b32 s61, s60, 0x8000
	s_mov_b32 m0, s27
	s_nop 0
	buffer_load_dwordx4 v166, s[12:15], s61 offen lds
	v_mfma_f32_16x16x32_bf16 v[132:135], v[52:55], v[148:151], v[132:135]
	s_waitcnt lgkmcnt(5)
	v_mfma_f32_16x16x32_bf16 v[136:139], v[56:59], v[152:155], v[136:139]
	v_mfma_f32_16x16x32_bf16 v[128:131], v[60:63], v[152:155], v[128:131]
	ds_read_b128 v[88:91], v124 offset:38912
	ds_read_b128 v[92:95], v124 offset:39168
	s_waitcnt lgkmcnt(6)
	v_mfma_f32_16x16x32_bf16 v[140:143], v[56:59], v[156:159], v[140:143]
	s_or_b32 s61, s60, 0xa000
	s_mov_b32 m0, s28
	s_nop 0
	buffer_load_dwordx4 v166, s[12:15], s61 offen lds
	v_mfma_f32_16x16x32_bf16 v[132:135], v[60:63], v[156:159], v[132:135]
	s_barrier
	ds_read_b128 v[144:147], v168 offset:32768
	ds_read_b128 v[148:151], v168 offset:33024
	ds_read_b128 v[152:155], v168 offset:34816
	ds_read_b128 v[156:159], v168 offset:35072
	ds_read_b128 v[224:227], v168 offset:36864
	s_waitcnt lgkmcnt(4)
	v_mfma_f32_16x16x32_bf16 v[208:211], v[64:67], v[144:147], v[208:211]
	v_mfma_f32_16x16x32_bf16 v[212:215], v[68:71], v[144:147], v[212:215]
	ds_read_b128 v[228:231], v168 offset:37120
	s_waitcnt lgkmcnt(4)
	v_mfma_f32_16x16x32_bf16 v[216:219], v[64:67], v[148:151], v[216:219]
	v_mfma_f32_16x16x32_bf16 v[220:223], v[68:71], v[148:151], v[220:223]
	ds_read_b128 v[144:147], v168 offset:38912
	s_waitcnt lgkmcnt(4)
	v_mfma_f32_16x16x32_bf16 v[208:211], v[72:75], v[152:155], v[208:211]
	v_mfma_f32_16x16x32_bf16 v[212:215], v[76:79], v[152:155], v[212:215]
	ds_read_b128 v[148:151], v168 offset:39168
	s_waitcnt lgkmcnt(4)
	v_mfma_f32_16x16x32_bf16 v[216:219], v[72:75], v[156:159], v[216:219]
	v_mfma_f32_16x16x32_bf16 v[220:223], v[76:79], v[156:159], v[220:223]
	s_waitcnt lgkmcnt(3)
	v_mfma_f32_16x16x32_bf16 v[208:211], v[80:83], v[224:227], v[208:211]
	v_mfma_f32_16x16x32_bf16 v[212:215], v[84:87], v[224:227], v[212:215]
	s_waitcnt lgkmcnt(2)
	v_mfma_f32_16x16x32_bf16 v[216:219], v[80:83], v[228:231], v[216:219]
	v_mfma_f32_16x16x32_bf16 v[220:223], v[84:87], v[228:231], v[220:223]
	s_waitcnt lgkmcnt(1)
	v_mfma_f32_16x16x32_bf16 v[208:211], v[88:91], v[144:147], v[208:211]
	v_mfma_f32_16x16x32_bf16 v[212:215], v[92:95], v[144:147], v[212:215]
	s_waitcnt lgkmcnt(0)
	v_mfma_f32_16x16x32_bf16 v[216:219], v[88:91], v[148:151], v[216:219]
	v_mfma_f32_16x16x32_bf16 v[220:223], v[92:95], v[148:151], v[220:223]
	s_waitcnt vmcnt(4)
	s_barrier
	ds_read_b128 v[152:155], v168 offset:40960
	ds_read_b128 v[156:159], v168 offset:41216
	ds_read_b128 v[224:227], v168 offset:43008
	ds_read_b128 v[228:231], v168 offset:43264
	ds_read_b128 v[144:147], v168 offset:45056
	ds_read_b128 v[96:99], v124 offset:40960
	ds_read_b128 v[100:103], v124 offset:41216
	ds_read_b128 v[104:107], v124 offset:43008
	ds_read_b128 v[108:111], v124 offset:43264
	s_waitcnt lgkmcnt(2)
	v_mfma_f32_16x16x32_bf16 v[208:211], v[96:99], v[152:155], v[208:211]
	v_mfma_f32_16x16x32_bf16 v[212:215], v[100:103], v[152:155], v[212:215]
	ds_read_b128 v[148:151], v168 offset:45312
	ds_read_b128 v[112:115], v124 offset:45056
	ds_read_b128 v[116:119], v124 offset:45312
	v_mfma_f32_16x16x32_bf16 v[216:219], v[96:99], v[156:159], v[216:219]
	v_mfma_f32_16x16x32_bf16 v[220:223], v[100:103], v[156:159], v[220:223]
	ds_read_b128 v[152:155], v168 offset:47104
	s_waitcnt lgkmcnt(4)
	v_mfma_f32_16x16x32_bf16 v[208:211], v[104:107], v[224:227], v[208:211]
	v_mfma_f32_16x16x32_bf16 v[212:215], v[108:111], v[224:227], v[212:215]
	ds_read_b128 v[156:159], v168 offset:47360
	ds_read_b128 v[120:123], v124 offset:47104
	ds_read_b128 v[124:127], v124 offset:47360
	v_mfma_f32_16x16x32_bf16 v[216:219], v[104:107], v[228:231], v[216:219]
	v_mfma_f32_16x16x32_bf16 v[220:223], v[108:111], v[228:231], v[220:223]
	s_waitcnt lgkmcnt(4)
	v_mfma_f32_16x16x32_bf16 v[208:211], v[112:115], v[144:147], v[208:211]
	v_mfma_f32_16x16x32_bf16 v[212:215], v[116:119], v[144:147], v[212:215]
	v_mfma_f32_16x16x32_bf16 v[216:219], v[112:115], v[148:151], v[216:219]
	v_mfma_f32_16x16x32_bf16 v[220:223], v[116:119], v[148:151], v[220:223]
	s_waitcnt lgkmcnt(0)
	v_mfma_f32_16x16x32_bf16 v[208:211], v[120:123], v[152:155], v[208:211]
	v_mfma_f32_16x16x32_bf16 v[212:215], v[124:127], v[152:155], v[212:215]
	v_mfma_f32_16x16x32_bf16 v[216:219], v[120:123], v[156:159], v[216:219]
	v_mfma_f32_16x16x32_bf16 v[220:223], v[124:127], v[156:159], v[220:223]
	s_waitcnt vmcnt(0)
	s_barrier
	s_nop 7
	s_nop 3
	s_cmp_lg_u32 s8, s43
	s_cbranch_scc1 .Ldiag0_done
	s_mov_b64 s[56:57], exec
	s_and_b64 exec, s[56:57], s[0:1]
	global_store_dword v[164:165], v208, off
	v_mov_b32_e32 v208, -1.0
	global_store_dword v[164:165], v220, off offset:64
	v_mov_b32_e32 v220, -1.0
	s_and_b64 exec, s[56:57], s[2:3]
	global_store_dword v[164:165], v209, off
	v_mov_b32_e32 v209, -1.0
	global_store_dword v[164:165], v221, off offset:64
	v_mov_b32_e32 v221, -1.0
	s_and_b64 exec, s[56:57], s[4:5]
	global_store_dword v[164:165], v210, off
	v_mov_b32_e32 v210, -1.0
	global_store_dword v[164:165], v222, off offset:64
	v_mov_b32_e32 v222, -1.0
	s_and_b64 exec, s[56:57], s[6:7]
	global_store_dword v[164:165], v211, off
	v_mov_b32_e32 v211, -1.0
	global_store_dword v[164:165], v223, off offset:64
	v_mov_b32_e32 v223, -1.0
	s_mov_b64 exec, s[56:57]
.Ldiag0_done:
	s_add_i32 s60, s45, 4
	s_and_b32 s60, s60, 28
	s_or_b32 s62, s60, 2
	s_lshl_b32 s60, s60, 15
	s_lshl_b32 s62, s62, 15
	ds_read_b128 v[144:147], v169 offset:32768
	ds_read_b128 v[148:151], v169 offset:33024
	ds_read_b128 v[152:155], v169 offset:34816
	ds_read_b128 v[156:159], v169 offset:35072
	ds_read_b128 v[224:227], v169 offset:36864
	s_waitcnt lgkmcnt(4)
	v_mfma_f32_16x16x32_bf16 v[136:139], v[64:67], v[144:147], v[136:139]
	v_mfma_f32_16x16x32_bf16 v[128:131], v[68:71], v[144:147], v[128:131]
	ds_read_b128 v[228:231], v169 offset:37120
	s_waitcnt lgkmcnt(4)
	v_mfma_f32_16x16x32_bf16 v[140:143], v[64:67], v[148:151], v[140:143]
	s_or_b32 s61, s60, 0x4000
	s_mov_b32 m0, s29
	s_nop 0
	buffer_load_dwordx4 v166, s[12:15], s61 offen lds
	v_mfma_f32_16x16x32_bf16 v[132:135], v[68:71], v[148:151], v[132:135]
	ds_read_b128 v[144:147], v169 offset:38912
	s_waitcnt lgkmcnt(4)
	v_mfma_f32_16x16x32_bf16 v[136:139], v[72:75], v[152:155], v[136:139]
	v_mfma_f32_16x16x32_bf16 v[128:131], v[76:79], v[152:155], v[128:131]
	ds_read_b128 v[148:151], v169 offset:39168
	v_and_or_b32 v237, v208, s49, v234
	v_and_or_b32 v238, v216, s49, v235
	v_max_f32_e32 v161, v237, v238
	s_waitcnt lgkmcnt(4)
	v_mfma_f32_16x16x32_bf16 v[140:143], v[72:75], v[156:159], v[140:143]
	s_or_b32 s61, s60, 0x6000
	s_mov_b32 m0, s30
	s_nop 0
	buffer_load_dwordx4 v166, s[12:15], s61 offen lds
	v_mfma_f32_16x16x32_bf16 v[132:135], v[76:79], v[156:159], v[132:135]
	ds_read_b128 v[152:155], v169 offset:40960
	v_and_or_b32 v237, v209, s49, v234
	v_and_or_b32 v238, v217, s49, v235
	v_max_f32_e32 v160, v237, v238
	s_waitcnt lgkmcnt(4)
	v_mfma_f32_16x16x32_bf16 v[136:139], v[80:83], v[224:227], v[136:139]
	v_mfma_f32_16x16x32_bf16 v[128:131], v[84:87], v[224:227], v[128:131]
	ds_read_b128 v[156:159], v169 offset:41216
	v_and_or_b32 v237, v210, s49, v234
	v_and_or_b32 v238, v218, s49, v235
	v_max_f32_e32 v162, v237, v238
	s_waitcnt lgkmcnt(4)
	v_mfma_f32_16x16x32_bf16 v[140:143], v[80:83], v[228:231], v[140:143]
	s_or_b32 s61, s60, 0xc000
	s_mov_b32 m0, s31
	s_nop 0
	buffer_load_dwordx4 v166, s[12:15], s61 offen lds
	v_mfma_f32_16x16x32_bf16 v[132:135], v[84:87], v[228:231], v[132:135]
	ds_read_b128 v[224:227], v169 offset:43008
	v_and_or_b32 v237, v211, s49, v234
	v_and_or_b32 v238, v219, s49, v235
	v_max_f32_e32 v163, v237, v238
	s_waitcnt lgkmcnt(4)
	v_mfma_f32_16x16x32_bf16 v[136:139], v[88:91], v[144:147], v[136:139]
	v_mfma_f32_16x16x32_bf16 v[128:131], v[92:95], v[144:147], v[128:131]
	ds_read_b128 v[228:231], v169 offset:43264
	v_and_or_b32 v237, v212, s49, v234
	v_and_or_b32 v238, v220, s49, v235
	v_max_f32_e32 v203, v237, v238
	s_waitcnt lgkmcnt(4)
	v_mfma_f32_16x16x32_bf16 v[140:143], v[88:91], v[148:151], v[140:143]
	s_or_b32 s61, s60, 0xe000
	s_mov_b32 m0, s33
	s_nop 0
	buffer_load_dwordx4 v166, s[12:15], s61 offen lds
	v_mfma_f32_16x16x32_bf16 v[132:135], v[92:95], v[148:151], v[132:135]
	ds_read_b128 v[144:147], v169 offset:45056
	v_and_or_b32 v237, v213, s49, v234
	v_and_or_b32 v238, v221, s49, v235
	v_max_f32_e32 v204, v237, v238
	s_waitcnt lgkmcnt(4)
	v_mfma_f32_16x16x32_bf16 v[136:139], v[96:99], v[152:155], v[136:139]
	v_mfma_f32_16x16x32_bf16 v[128:131], v[100:103], v[152:155], v[128:131]
	ds_read_b128 v[148:151], v169 offset:45312
	v_and_or_b32 v237, v214, s49, v234
	v_and_or_b32 v238, v222, s49, v235
	v_max_f32_e32 v205, v237, v238
	s_waitcnt lgkmcnt(4)
	v_mfma_f32_16x16x32_bf16 v[140:143], v[96:99], v[156:159], v[140:143]
	s_mov_b32 s61, s62
	s_mov_b32 m0, s34
	s_nop 0
	buffer_load_dwordx4 v166, s[12:15], s61 offen lds
	v_mfma_f32_16x16x32_bf16 v[132:135], v[100:103], v[156:159], v[132:135]
	ds_read_b128 v[152:155], v169 offset:47104
	v_and_or_b32 v237, v215, s49, v234
	v_and_or_b32 v238, v223, s49, v235
	v_max_f32_e32 v206, v237, v238
	s_waitcnt lgkmcnt(4)
	v_mfma_f32_16x16x32_bf16 v[136:139], v[104:107], v[224:227], v[136:139]
	v_mfma_f32_16x16x32_bf16 v[128:131], v[108:111], v[224:227], v[128:131]
	ds_read_b128 v[156:159], v169 offset:47360
	s_waitcnt lgkmcnt(4)
	v_mfma_f32_16x16x32_bf16 v[140:143], v[104:107], v[228:231], v[140:143]
	s_or_b32 s61, s62, 0x2000
	s_mov_b32 m0, s35
	s_nop 0
	buffer_load_dwordx4 v166, s[12:15], s61 offen lds
	v_mfma_f32_16x16x32_bf16 v[132:135], v[108:111], v[228:231], v[132:135]
	s_waitcnt lgkmcnt(3)
	v_mfma_f32_16x16x32_bf16 v[136:139], v[112:115], v[144:147], v[136:139]
	v_mfma_f32_16x16x32_bf16 v[128:131], v[116:119], v[144:147], v[128:131]
	s_waitcnt lgkmcnt(2)
	v_mfma_f32_16x16x32_bf16 v[140:143], v[112:115], v[148:151], v[140:143]
	s_or_b32 s61, s62, 0x8000
	s_mov_b32 m0, s36
	s_nop 0
	buffer_load_dwordx4 v166, s[12:15], s61 offen lds
	v_mfma_f32_16x16x32_bf16 v[132:135], v[116:119], v[148:151], v[132:135]
	s_waitcnt lgkmcnt(1)
	v_mfma_f32_16x16x32_bf16 v[136:139], v[120:123], v[152:155], v[136:139]
	v_mfma_f32_16x16x32_bf16 v[128:131], v[124:127], v[152:155], v[128:131]
	s_waitcnt lgkmcnt(0)
	v_mfma_f32_16x16x32_bf16 v[140:143], v[120:123], v[156:159], v[140:143]
	s_or_b32 s61, s62, 0xa000
	s_mov_b32 m0, s37
	s_nop 0
	buffer_load_dwordx4 v166, s[12:15], s61 offen lds
	v_mfma_f32_16x16x32_bf16 v[132:135], v[124:127], v[156:159], v[132:135]
	v_lshl_or_b32 v202, v167, 2, s47
	v_add_u32_e32 v202, 0x1ff00, v202
	s_add_i32 s50, s50, -4
	s_mov_b32 s51, -1.0
	s_movk_i32 s52, 0xff80
	s_brev_b32 s53, -2
	ds_read_b128 v[144:147], v168
	ds_read_b128 v[148:151], v168 offset:256
	ds_read_b128 v[152:155], v168 offset:2048
	ds_read_b128 v[156:159], v168 offset:2304
	s_branch .LBB3_13
